# loader waves stagger their ring writes (s_sleep between the W / K / u groups) so the MFMA waves' fragment reads go first
# speedup vs baseline: 1.0081x; 1.0053x over previous
; DI bf16x8 packS(const f32x16& x, int s) { return pack8(x[8 * s], x[8 * s + 1], x[8 * s + 2], x[8 * s + 3], x[8 * s + 4], x[8 * s + 5], x[8 * s + 6], x[8 * s + 7]); }
; DI void gdn_scan_seq(const Params& p, int bh16, char* ldsf) {
;     ...
;   f32x16 S[4];
; #pragma unroll
;   for (int m = 0; m < 4; ++m)
; #pragma unroll
;     for (int r = 0; r < 16; ++r) S[m][r] = 0.f;
;   asm volatile("s_waitcnt vmcnt(0)" ::: "memory");
;   __syncthreads();
;   SCAN_ISSUE(0, 0); SCAN_ISSUE(1, 1);
;   int sl = 0;
; #pragma unroll 1
;   for (int c = 0; c < 128; ++c) {
;     if (c + 1 < 128) asm volatile("s_waitcnt vmcnt(12)" ::: "memory"); else asm volatile("s_waitcnt vmcnt(0)" ::: "memory");
;     __builtin_amdgcn_s_barrier();
;     asm volatile("" ::: "memory");
;     char* sco = scp + (size_t)c * 32768;
;     bf16x8 Sb[4][2];
; #pragma unroll
;     for (int m = 0; m < 4; ++m) { Sb[m][0] = packS(S[m], 0); Sb[m][1] = packS(S[m], 1); *(bf16x8*)(sco + (m * 2 + 0) * 1024) = Sb[m][0]; *(bf16x8*)(sco + (m * 2 + 1) * 1024) = Sb[m][1]; }
;     __builtin_amdgcn_sched_barrier(0);
;     if (c + 2 < 128) { const int s2 = sl >= 1 ? sl - 1 : 2; SCAN_ISSUE(c + 2, s2); }
; DI void phase_mixer(const Params& p, int bid, int nb, char* lds, char* ctl, char* ldsf) {
;     ...
;   if (bid < 32) { if (vb == 0) gdn_scan_seq(p, bid >> 1, ldsf); else { __syncthreads(); for (int k = 0; k < 128; ++k) { __builtin_amdgcn_s_barrier(); asm volatile("" ::: "memory"); } __syncthreads(); } }
.Lshadow_loop:
	s_waitcnt vmcnt(36)
	v_add_u32_e32 v209, s3, v208
	v_add_u32_e32 v211, s3, v210
	s_sleep 4
	ds_write_b128 v209, v[0:3]
	ds_write_b128 v209, v[4:7] offset:1024
	ds_write_b128 v209, v[8:11] offset:2048
	ds_write_b128 v209, v[12:15] offset:3072
	s_sleep 3
	ds_write_b128 v209, v[16:19] offset:16384
	ds_write_b128 v209, v[20:23] offset:17408
	ds_write_b128 v209, v[24:27] offset:18432
	ds_write_b128 v209, v[28:31] offset:19456
	s_sleep 3
	s_mov_b64 exec, s[16:17]
	ds_write_b128 v211, v[32:35] offset:32768
	ds_write_b128 v211, v[36:39] offset:33792
	ds_write_b128 v211, v[40:43] offset:34816
	ds_write_b128 v211, v[44:47] offset:35840
	s_mov_b64 exec, -1
	global_load_dwordx4 v[0:3], v132, s[8:9]
	global_load_dwordx4 v[4:7], v132, s[8:9] offset:1024
	global_load_dwordx4 v[8:11], v132, s[8:9] offset:2048
	global_load_dwordx4 v[12:15], v132, s[8:9] offset:3072
	global_load_dwordx4 v[16:19], v132, s[10:11]
	global_load_dwordx4 v[20:23], v132, s[10:11] offset:1024
	global_load_dwordx4 v[24:27], v132, s[10:11] offset:2048
	global_load_dwordx4 v[28:31], v132, s[10:11] offset:3072
	global_load_dwordx4 v[32:35], v133, s[12:13]
	global_load_dwordx4 v[36:39], v133, s[12:13] offset:16
	global_load_dwordx4 v[40:43], v134, s[12:13]
	global_load_dwordx4 v[44:47], v134, s[12:13] offset:16
	s_add_u32 s15, s15, 1
	s_cmp_lt_u32 s15, 0x80
	s_cselect_b32 s14, 0x4000, 0
	s_add_u32 s8, s8, s14
	s_addc_u32 s9, s9, 0
	s_add_u32 s10, s10, s14
	s_addc_u32 s11, s11, 0
	s_add_u32 s12, s12, s14
	s_addc_u32 s13, s13, 0
	s_xor_b32 s3, s3, 0xc000
	s_waitcnt lgkmcnt(0)
	s_barrier
	s_waitcnt vmcnt(36)
	v_add_u32_e32 v209, s3, v208
	v_add_u32_e32 v211, s3, v210
	s_sleep 4
	ds_write_b128 v209, v[48:51]
	ds_write_b128 v209, v[52:55] offset:1024
	ds_write_b128 v209, v[56:59] offset:2048
	ds_write_b128 v209, v[60:63] offset:3072
	s_sleep 3
	ds_write_b128 v209, v[64:67] offset:16384
	ds_write_b128 v209, v[68:71] offset:17408
	ds_write_b128 v209, v[72:75] offset:18432
	ds_write_b128 v209, v[76:79] offset:19456
	s_sleep 3
	s_mov_b64 exec, s[16:17]
	ds_write_b128 v211, v[80:83] offset:32768
	ds_write_b128 v211, v[84:87] offset:33792
	ds_write_b128 v211, v[88:91] offset:34816
	ds_write_b128 v211, v[92:95] offset:35840
	s_mov_b64 exec, -1
	global_load_dwordx4 v[48:51], v132, s[8:9]
	global_load_dwordx4 v[52:55], v132, s[8:9] offset:1024
	global_load_dwordx4 v[56:59], v132, s[8:9] offset:2048
	global_load_dwordx4 v[60:63], v132, s[8:9] offset:3072
	global_load_dwordx4 v[64:67], v132, s[10:11]
	global_load_dwordx4 v[68:71], v132, s[10:11] offset:1024
	global_load_dwordx4 v[72:75], v132, s[10:11] offset:2048
	global_load_dwordx4 v[76:79], v132, s[10:11] offset:3072
	global_load_dwordx4 v[80:83], v133, s[12:13]
	global_load_dwordx4 v[84:87], v133, s[12:13] offset:16
	global_load_dwordx4 v[88:91], v134, s[12:13]
	global_load_dwordx4 v[92:95], v134, s[12:13] offset:16
	s_add_u32 s15, s15, 1
	s_cmp_lt_u32 s15, 0x80
	s_cselect_b32 s14, 0x4000, 0
	s_add_u32 s8, s8, s14
	s_addc_u32 s9, s9, 0
	s_add_u32 s10, s10, s14
	s_addc_u32 s11, s11, 0
	s_add_u32 s12, s12, s14
	s_addc_u32 s13, s13, 0
	s_xor_b32 s3, s3, 0xc000
	s_waitcnt lgkmcnt(0)
	s_barrier
	s_waitcnt vmcnt(36)
	v_add_u32_e32 v209, s3, v208
	v_add_u32_e32 v211, s3, v210
	s_sleep 4
	ds_write_b128 v209, v[96:99]
	ds_write_b128 v209, v[100:103] offset:1024
	ds_write_b128 v209, v[104:107] offset:2048
	ds_write_b128 v209, v[108:111] offset:3072
	s_sleep 3
	ds_write_b128 v209, v[112:115] offset:16384
	ds_write_b128 v209, v[116:119] offset:17408
	ds_write_b128 v209, v[120:123] offset:18432
	ds_write_b128 v209, v[124:127] offset:19456
	s_sleep 3
	s_mov_b64 exec, s[16:17]
	ds_write_b128 v211, v[128:131] offset:32768
	ds_write_b128 v211, v[136:139] offset:33792
	ds_write_b128 v211, v[140:143] offset:34816
	ds_write_b128 v211, v[148:151] offset:35840
	s_mov_b64 exec, -1
	global_load_dwordx4 v[96:99], v132, s[8:9]
	global_load_dwordx4 v[100:103], v132, s[8:9] offset:1024
	global_load_dwordx4 v[104:107], v132, s[8:9] offset:2048
	global_load_dwordx4 v[108:111], v132, s[8:9] offset:3072
	global_load_dwordx4 v[112:115], v132, s[10:11]
	global_load_dwordx4 v[116:119], v132, s[10:11] offset:1024
	global_load_dwordx4 v[120:123], v132, s[10:11] offset:2048
	global_load_dwordx4 v[124:127], v132, s[10:11] offset:3072
	global_load_dwordx4 v[128:131], v133, s[12:13]
	global_load_dwordx4 v[136:139], v133, s[12:13] offset:16
	global_load_dwordx4 v[140:143], v134, s[12:13]
	global_load_dwordx4 v[148:151], v134, s[12:13] offset:16
	s_add_u32 s15, s15, 1
	s_cmp_lt_u32 s15, 0x80
	s_cselect_b32 s14, 0x4000, 0
	s_add_u32 s8, s8, s14
	s_addc_u32 s9, s9, 0
	s_add_u32 s10, s10, s14
	s_addc_u32 s11, s11, 0
	s_add_u32 s12, s12, s14
	s_addc_u32 s13, s13, 0
	s_xor_b32 s3, s3, 0xc000
	s_waitcnt lgkmcnt(0)
	s_barrier
	s_waitcnt vmcnt(36)
	v_add_u32_e32 v209, s3, v208
	v_add_u32_e32 v211, s3, v210
	s_sleep 4
	ds_write_b128 v209, v[152:155]
	ds_write_b128 v209, v[156:159] offset:1024
	ds_write_b128 v209, v[160:163] offset:2048
	ds_write_b128 v209, v[164:167] offset:3072
	s_sleep 3
	ds_write_b128 v209, v[168:171] offset:16384
	ds_write_b128 v209, v[172:175] offset:17408
	ds_write_b128 v209, v[178:181] offset:18432
	ds_write_b128 v209, v[182:185] offset:19456
	s_sleep 3
	s_mov_b64 exec, s[16:17]
	ds_write_b128 v211, v[190:193] offset:32768
	ds_write_b128 v211, v[194:197] offset:33792
	ds_write_b128 v211, v[198:201] offset:34816
	ds_write_b128 v211, v[202:205] offset:35840
	s_mov_b64 exec, -1
	global_load_dwordx4 v[152:155], v132, s[8:9]
	global_load_dwordx4 v[156:159], v132, s[8:9] offset:1024
	global_load_dwordx4 v[160:163], v132, s[8:9] offset:2048
	global_load_dwordx4 v[164:167], v132, s[8:9] offset:3072
	global_load_dwordx4 v[168:171], v132, s[10:11]
	global_load_dwordx4 v[172:175], v132, s[10:11] offset:1024
	global_load_dwordx4 v[178:181], v132, s[10:11] offset:2048
	global_load_dwordx4 v[182:185], v132, s[10:11] offset:3072
	global_load_dwordx4 v[190:193], v133, s[12:13]
	global_load_dwordx4 v[194:197], v133, s[12:13] offset:16
	global_load_dwordx4 v[198:201], v134, s[12:13]
	global_load_dwordx4 v[202:205], v134, s[12:13] offset:16
	s_add_u32 s15, s15, 1
	s_cmp_lt_u32 s15, 0x80
	s_cselect_b32 s14, 0x4000, 0
	s_add_u32 s8, s8, s14
	s_addc_u32 s9, s9, 0
	s_add_u32 s10, s10, s14
	s_addc_u32 s11, s11, 0
	s_add_u32 s12, s12, s14
	s_addc_u32 s13, s13, 0
	s_xor_b32 s3, s3, 0xc000
	s_waitcnt lgkmcnt(0)
	s_barrier
	s_add_u32 s2, s2, 1
	s_cmp_lt_u32 s2, 32
	s_cbranch_scc1 .Lshadow_loop
	s_waitcnt vmcnt(0)
	s_barrier
